# attention: light waves (0-3) start each active tile s_sleep 12 later (half-tile stagger against the heavy SIMD partner), with the read-ahead QK block
# speedup vs baseline: 1.0950x; 1.0950x over previous
; #define LAS __attribute__((address_space(3)))
; #define SBAR() __builtin_amdgcn_sched_barrier(0)
; __device__ __forceinline__ void qkt(f32x16& p0, f32x16& p1, LAS unsigned char* lds  , int r32, int hi, const bf16x8* qr) {
;     p0 = f32x16{}; p1 = f32x16{};
;     const LAS unsigned char* kb[4];
; #pragma unroll
;     for (int dd = 0; dd < 4; ++dd) kb[dd] = lds + K_OFF + KSWZ(r32, (dd * 16 + hi * 8) * 2);
; #pragma unroll
;     for (int d0 = 0; d0 < 8; ++d0) { const LAS unsigned char* a = kb[d0 & 3] + (d0 >> 2) * 128;
;         const bf16x8 b0 = *(const LAS bf16x8*)(a);
;         const bf16x8 b1 = *(const LAS bf16x8*)(a + 32 * 256);
;         p0 = __builtin_amdgcn_mfma_f32_32x32x16_bf16(b0, qr[d0], p0, 0, 0, 0);
;         p1 = __builtin_amdgcn_mfma_f32_32x32x16_bf16(b1, qr[d0], p1, 0, 0, 0); }
; #pragma unroll
;     for (int e = 0; e < 4; ++e) { const LAS unsigned char* a = lds + P_OFF + KPSWZ(r32, (e * 2 + hi) * 16);
;         const bf16x8 b0 = *(const LAS bf16x8*)(a);
;         const bf16x8 b1 = *(const LAS bf16x8*)(a + 32 * 128);
;         p0 = __builtin_amdgcn_mfma_f32_32x32x16_bf16(b0, qr[8 + e], p0, 0, 0, 0);
;         p1 = __builtin_amdgcn_mfma_f32_32x32x16_bf16(b1, qr[8 + e], p1, 0, 0, 0); }
; }
; __device__ __forceinline__ void attn_unit(LAS unsigned char* lds, int b, int h, int qb, const bf16* Q  , const bf16* KV  , const bf16* KPE  ,
;                                           const float* ROPE  , bf16* O  , const int wave_) {
;     ...
;     for (int t = 0; t < NT; ++t) {
;         asm volatile("s_waitcnt vmcnt(5)" ::: "memory"); __builtin_amdgcn_s_barrier();
;         { const int tn = (t + 2 < NT) ? t + 2 : NT - 1; AISSUE(tn, bl); }
;         const int kb_ = t * KVBLK;
;         if (kb_ <= qlo + 31) {
;             SBAR(); qkt(p0, p1, lds + bc, r32, hi, qr);
.LBB0_720:
	s_add_i32 s4, s73, 2
	s_min_u32 s70, s4, s2
	s_lshl_b64 s[4:5], s[70:71], 18
	s_add_u32 s4, s96, s4
	s_addc_u32 s5, s97, s5
	v_lshl_add_u64 v[64:65], v[150:151], 1, s[4:5]
	s_add_i32 s8, s95, s69
	v_lshl_add_u64 v[64:65], v[64:65], 0, s[66:67]
	s_mov_b32 m0, s8
	s_waitcnt vmcnt(5)
	s_barrier
	global_load_lds_dwordx4 v[64:65], off
	v_lshl_add_u64 v[64:65], v[152:153], 1, s[4:5]
	v_lshl_add_u64 v[64:65], v[64:65], 0, s[66:67]
	s_add_i32 m0, s8, 0x2000
	s_lshl_b64 s[6:7], s[70:71], 13
	global_load_lds_dwordx4 v[64:65], off
	v_lshl_add_u64 v[64:65], v[146:147], 1, s[4:5]
	s_add_i32 m0, s8, 0x4000
	s_nop 0
	global_load_lds_dwordx4 v[64:65], off
	v_lshl_add_u64 v[64:65], v[148:149], 1, s[4:5]
	s_add_i32 m0, s8, 0x6000
	s_sub_i32 s4, s94, 63
	global_load_lds_dwordx4 v[64:65], off
	v_lshl_add_u64 v[64:65], v[154:155], 0, s[6:7]
	s_add_i32 m0, s8, 0x8000
	s_cmp_gt_i32 s4, s68
	global_load_lds_dwordx4 v[64:65], off
	s_cbranch_scc1 .LBB0_728
	v_readlane_b32 s4, v254, 60
	s_nop 3
	s_cmp_gt_u32 s4, 3
	s_cbranch_scc1 .Lattn_nodelay
	s_sleep 12
.Lattn_nodelay:
	s_add_i32 s4, s72, 0
	v_add_u32_e32 v216, s4, v160
	v_add_u32_e32 v220, s4, v166
	v_add_u32_e32 v217, v216, v162
	v_add_u32_e32 v218, v216, v163
	v_add_u32_e32 v219, v216, v165
	v_add_u32_e32 v216, v216, v161
	v_add_u32_e32 v221, v220, v168
	v_add_u32_e32 v222, v220, v169
	v_add_u32_e32 v223, v220, v170
	v_add_u32_e32 v220, v220, v167
	ds_read_b128 v[176:179], v216 offset:16384
	ds_read_b128 v[180:183], v216 offset:24576
	ds_read_b128 v[184:187], v217 offset:16384
	ds_read_b128 v[188:191], v217 offset:24576
	ds_read_b128 v[192:195], v218 offset:16384
	ds_read_b128 v[196:199], v218 offset:24576
	ds_read_b128 v[200:203], v219 offset:16384
	ds_read_b128 v[204:207], v219 offset:24576
	s_cmp_le_i32 s94, s33
	ds_read_b128 v[208:211], v216 offset:16512
	ds_read_b128 v[212:215], v216 offset:24704
	s_waitcnt lgkmcnt(8)
	v_mfma_f32_32x32x16_bf16 v[80:95], v[176:179], v[124:127], 0
	v_mfma_f32_32x32x16_bf16 v[64:79], v[180:183], v[124:127], 0
	ds_read_b128 v[176:179], v217 offset:16512
	ds_read_b128 v[180:183], v217 offset:24704
	s_waitcnt lgkmcnt(8)
	v_mfma_f32_32x32x16_bf16 v[80:95], v[184:187], v[100:103], v[80:95]
	v_mfma_f32_32x32x16_bf16 v[64:79], v[188:191], v[100:103], v[64:79]
	ds_read_b128 v[184:187], v218 offset:16512
	ds_read_b128 v[188:191], v218 offset:24704
	s_waitcnt lgkmcnt(8)
	v_mfma_f32_32x32x16_bf16 v[80:95], v[192:195], v[104:107], v[80:95]
	v_mfma_f32_32x32x16_bf16 v[64:79], v[196:199], v[104:107], v[64:79]
	ds_read_b128 v[192:195], v219 offset:16512
	ds_read_b128 v[196:199], v219 offset:24704
	s_waitcnt lgkmcnt(8)
	v_mfma_f32_32x32x16_bf16 v[80:95], v[200:203], v[108:111], v[80:95]
	v_mfma_f32_32x32x16_bf16 v[64:79], v[204:207], v[108:111], v[64:79]
	ds_read_b128 v[200:203], v220 offset:32768
	ds_read_b128 v[204:207], v220 offset:36864
	s_waitcnt lgkmcnt(8)
	v_mfma_f32_32x32x16_bf16 v[80:95], v[208:211], v[112:115], v[80:95]
	v_mfma_f32_32x32x16_bf16 v[64:79], v[212:215], v[112:115], v[64:79]
	ds_read_b128 v[208:211], v221 offset:32768
	ds_read_b128 v[212:215], v221 offset:36864
	s_waitcnt lgkmcnt(8)
	v_mfma_f32_32x32x16_bf16 v[80:95], v[176:179], v[116:119], v[80:95]
	v_mfma_f32_32x32x16_bf16 v[64:79], v[180:183], v[116:119], v[64:79]
	ds_read_b128 v[176:179], v222 offset:32768
	ds_read_b128 v[180:183], v222 offset:36864
	s_waitcnt lgkmcnt(8)
	v_mfma_f32_32x32x16_bf16 v[80:95], v[184:187], v[120:123], v[80:95]
	v_mfma_f32_32x32x16_bf16 v[64:79], v[188:191], v[120:123], v[64:79]
	ds_read_b128 v[184:187], v223 offset:32768
	ds_read_b128 v[188:191], v223 offset:36864
	s_waitcnt lgkmcnt(8)
	v_mfma_f32_32x32x16_bf16 v[80:95], v[192:195], v[96:99], v[80:95]
	v_mfma_f32_32x32x16_bf16 v[64:79], v[196:199], v[96:99], v[64:79]
	s_waitcnt lgkmcnt(6)
	v_mfma_f32_32x32x16_bf16 v[80:95], v[200:203], v[128:131], v[80:95]
	v_mfma_f32_32x32x16_bf16 v[64:79], v[204:207], v[128:131], v[64:79]
	s_waitcnt lgkmcnt(4)
	v_mfma_f32_32x32x16_bf16 v[80:95], v[208:211], v[136:139], v[80:95]
	v_mfma_f32_32x32x16_bf16 v[64:79], v[212:215], v[136:139], v[64:79]
	s_waitcnt lgkmcnt(2)
	v_mfma_f32_32x32x16_bf16 v[80:95], v[176:179], v[132:135], v[80:95]
	v_mfma_f32_32x32x16_bf16 v[64:79], v[180:183], v[132:135], v[64:79]
	s_waitcnt lgkmcnt(0)
	v_mfma_f32_32x32x16_bf16 v[80:95], v[184:187], v[140:143], v[80:95]
	v_mfma_f32_32x32x16_bf16 v[64:79], v[188:191], v[140:143], v[64:79]
	s_cbranch_scc1 .LBB0_723
; __device__ __forceinline__ void mask_tile(f32x16& p0, f32x16& p1, int dq) {
;     const float NEG = -__builtin_inff();
; #pragma unroll
;     for (int r = 0; r < 16; ++r) { const int c = (r & 3) + 8 * (r >> 2);
;         if (dq - c < 0) p0[r] = NEG;
;         if (dq - c - 32 < 0) p1[r] = NEG; }
; }
	v_cmp_gt_i32_e64 s[62:63], 26, v172
	v_cmp_gt_i32_e64 s[64:65], 27, v172
	v_cmp_gt_i32_e64 s[60:61], 25, v172
	s_and_b64 s[62:63], s[64:65], s[62:63]
	v_cmp_gt_i32_e64 s[58:59], 24, v172
	s_and_b64 s[60:61], s[62:63], s[60:61]
	v_cmp_gt_i32_e64 s[56:57], 19, v172
	s_and_b64 s[58:59], s[60:61], s[58:59]
	v_cmp_gt_i32_e64 s[54:55], 18, v172
	s_and_b64 s[56:57], s[58:59], s[56:57]
	v_cmp_gt_i32_e64 s[52:53], 17, v172
	s_and_b64 s[54:55], s[56:57], s[54:55]
	v_cmp_gt_i32_e64 s[50:51], 16, v172
	s_and_b64 s[52:53], s[54:55], s[52:53]
	v_cmp_gt_i32_e64 s[48:49], 11, v172
	s_and_b64 s[50:51], s[52:53], s[50:51]
	v_cmp_gt_i32_e64 s[46:47], 10, v172
	s_and_b64 s[48:49], s[50:51], s[48:49]
	v_cmp_gt_i32_e64 s[44:45], 9, v172
	s_and_b64 s[46:47], s[48:49], s[46:47]
	v_cmp_gt_i32_e64 s[42:43], 8, v172
	s_and_b64 s[44:45], s[46:47], s[44:45]
	v_cmp_gt_i32_e64 s[40:41], 3, v172
	s_and_b64 s[42:43], s[44:45], s[42:43]
	v_cmp_gt_i32_e64 s[38:39], 2, v172
	s_and_b64 s[40:41], s[42:43], s[40:41]
	v_cmp_gt_i32_e64 s[36:37], 1, v172
	s_and_b64 s[38:39], s[40:41], s[38:39]
	v_cmp_gt_i32_e64 s[34:35], 0, v172
	s_and_b64 s[36:37], s[38:39], s[36:37]
	s_and_b64 s[34:35], s[36:37], s[34:35]
	v_cmp_gt_i32_e64 s[30:31], 58, v172
	v_cndmask_b32_e64 v80, v80, v173, s[34:35]
	v_cmp_gt_i32_e64 s[34:35], 59, v172
	v_cmp_gt_i32_e64 s[28:29], 57, v172
	s_and_b64 s[30:31], s[34:35], s[30:31]
	v_cmp_gt_i32_e64 s[26:27], 56, v172
	s_and_b64 s[28:29], s[30:31], s[28:29]
	v_cmp_gt_i32_e64 s[24:25], 51, v172
	s_and_b64 s[26:27], s[28:29], s[26:27]
	v_cmp_gt_i32_e64 s[22:23], 50, v172
	s_and_b64 s[24:25], s[26:27], s[24:25]
	v_cmp_gt_i32_e64 s[20:21], 49, v172
	s_and_b64 s[22:23], s[24:25], s[22:23]
	v_cmp_gt_i32_e64 s[18:19], 48, v172
	s_and_b64 s[20:21], s[22:23], s[20:21]
	v_cmp_gt_i32_e64 s[16:17], 43, v172
	s_and_b64 s[18:19], s[20:21], s[18:19]
	v_cmp_gt_i32_e64 s[14:15], 42, v172
	s_and_b64 s[16:17], s[18:19], s[16:17]
	v_cmp_gt_i32_e64 s[12:13], 41, v172
	s_and_b64 s[14:15], s[16:17], s[14:15]
	v_cmp_gt_i32_e64 s[10:11], 40, v172
	s_and_b64 s[12:13], s[14:15], s[12:13]
	v_cmp_gt_i32_e64 s[8:9], 35, v172
	s_and_b64 s[10:11], s[12:13], s[10:11]
	v_cmp_gt_i32_e64 s[6:7], 34, v172
	s_and_b64 s[8:9], s[10:11], s[8:9]
	v_cmp_gt_i32_e64 s[4:5], 33, v172
	v_cndmask_b32_e64 v94, v94, v173, s[62:63]
	v_cndmask_b32_e64 v93, v93, v173, s[60:61]
	v_cndmask_b32_e64 v92, v92, v173, s[58:59]
	v_cndmask_b32_e64 v91, v91, v173, s[56:57]
	v_cndmask_b32_e64 v90, v90, v173, s[54:55]
	v_cndmask_b32_e64 v89, v89, v173, s[52:53]
	v_cndmask_b32_e64 v88, v88, v173, s[50:51]
	v_cndmask_b32_e64 v87, v87, v173, s[48:49]
	v_readlane_b32 s48, v254, 42
	s_and_b64 s[6:7], s[8:9], s[6:7]
	v_cmp_gt_i32_e32 vcc, 32, v172
	v_readlane_b32 s52, v254, 46
	v_readlane_b32 s53, v254, 47
	v_readlane_b32 s56, v254, 50
	v_readlane_b32 s57, v254, 51
	v_readlane_b32 s58, v254, 52
	v_readlane_b32 s59, v254, 53
	v_readlane_b32 s60, v254, 54
	v_readlane_b32 s61, v254, 55
	s_and_b64 s[4:5], s[6:7], s[4:5]
	v_readlane_b32 s62, v254, 56
	v_readlane_b32 s63, v254, 57
	s_mov_b64 s[52:53], s[56:57]
	s_mov_b64 s[56:57], s[60:61]
	s_and_b64 vcc, s[4:5], vcc
	v_cndmask_b32_e64 v95, v95, v173, s[64:65]
	s_mov_b64 s[58:59], s[62:63]
	v_cndmask_b32_e64 v86, v86, v173, s[46:47]
	v_cndmask_b32_e64 v85, v85, v173, s[44:45]
	v_cndmask_b32_e64 v84, v84, v173, s[42:43]
	v_cndmask_b32_e64 v83, v83, v173, s[40:41]
	v_cndmask_b32_e64 v82, v82, v173, s[38:39]
	v_cndmask_b32_e64 v81, v81, v173, s[36:37]
	v_cndmask_b32_e64 v79, v79, v173, s[34:35]
	v_cndmask_b32_e64 v78, v78, v173, s[30:31]
	v_cndmask_b32_e64 v77, v77, v173, s[28:29]
	v_cndmask_b32_e64 v76, v76, v173, s[26:27]
	v_cndmask_b32_e64 v75, v75, v173, s[24:25]
	v_cndmask_b32_e64 v74, v74, v173, s[22:23]
	v_cndmask_b32_e64 v73, v73, v173, s[20:21]
	v_cndmask_b32_e64 v72, v72, v173, s[18:19]
	v_cndmask_b32_e64 v71, v71, v173, s[16:17]
	v_cndmask_b32_e64 v70, v70, v173, s[14:15]
	v_cndmask_b32_e64 v69, v69, v173, s[12:13]
	v_cndmask_b32_e64 v68, v68, v173, s[10:11]
	v_cndmask_b32_e64 v67, v67, v173, s[8:9]
	v_cndmask_b32_e64 v66, v66, v173, s[6:7]
	v_cndmask_b32_e64 v65, v65, v173, s[4:5]
	v_cndmask_b32_e32 v64, v64, v173, vcc
	v_readlane_b32 s49, v254, 43
	v_readlane_b32 s50, v254, 44
	v_readlane_b32 s51, v254, 45
	v_readlane_b32 s54, v254, 48
	v_readlane_b32 s55, v254, 49
